# t3_revident
# speedup vs baseline: 1.0703x; 1.0703x over previous
_Z11align_fusedPKfS0_PKiPf:
	s_load_dwordx2 s[6:7], s[0:1], 0x0
	s_sub_u32 s2, 0x1fff, s2
	s_mul_hi_u32 s3, s2, 0x1770
	s_mulk_i32 s2, 0x1770
	s_lshl_b64 s[4:5], s[2:3], 2
	s_waitcnt lgkmcnt(0)
	s_add_u32 s2, s6, s4
	s_addc_u32 s3, s7, s5
	v_mov_b32_e32 v31, 0
	v_lshlrev_b32_e32 v30, 4, v0
	v_lshl_add_u64 v[10:11], s[2:3], 0, v[30:31]
	s_movk_i32 s7, 0x2000
	v_add_co_u32_e32 v12, vcc, s7, v10
	s_movk_i32 s7, 0x3000
	s_nop 0
	v_addc_co_u32_e32 v13, vcc, 0, v11, vcc
	v_add_co_u32_e32 v18, vcc, s7, v10
	s_movk_i32 s6, 0xdc
	s_nop 0
	v_addc_co_u32_e32 v19, vcc, 0, v11, vcc
	v_add_co_u32_e32 v20, vcc, 0x4000, v10
	v_or_b32_e32 v48, 0x400, v0
	s_nop 0
	v_addc_co_u32_e32 v21, vcc, 0, v11, vcc
	v_or_b32_e32 v1, 0x500, v0
	v_cmp_gt_u32_e32 vcc, s6, v0
	global_load_dwordx4 v[2:5], v[12:13], off offset:-4096 nt
	global_load_dwordx4 v[6:9], v[12:13], off nt
	v_cndmask_b32_e32 v1, v48, v1, vcc
	global_load_dwordx4 v[10:13], v[18:19], off nt
	global_load_dwordx4 v[14:17], v[20:21], off nt
	v_lshlrev_b32_e32 v49, 4, v1
	global_load_dwordx4 v[22:25], v30, s[2:3] nt
	global_load_dwordx4 v[18:21], v49, s[2:3] nt
	v_and_b32_e32 v29, 63, v0
	v_cmp_gt_u32_e32 vcc, 64, v0
	v_mov_b32_e32 v26, v31
	v_mov_b32_e32 v27, v31
	v_mov_b32_e32 v28, v31
	s_and_saveexec_b64 s[2:3], vcc
	s_cbranch_execz .LBB0_2
	s_load_dwordx4 s[8:11], s[0:1], 0x8
	v_mul_u32_u24_e32 v1, 3, v29
	v_lshlrev_b32_e32 v31, 2, v29
	v_lshlrev_b32_e32 v1, 2, v1
	s_waitcnt lgkmcnt(0)
	global_load_dword v32, v31, s[10:11]
	global_load_dwordx3 v[26:28], v1, s[8:9] nt
	s_waitcnt vmcnt(1)
	v_lshl_add_u32 v31, v32, 1, v32
